# attention: rebase test on per-lane partial maxima; cross-half max swap (permlane + 3 v_max) moved into the rare rebase path
# baseline (speedup 1.0000x reference)
; __device__ __forceinline__ float swap_max(float v) { float r0, r1; swap32(v, r0, r1); return fmaxf(r0, r1); }
; __device__ __forceinline__ void attn_unit(const Frame& F, const bf16* __restrict__ proj, bf16* mix, const float* relb, const float* subg, int h, int qb, float lam, float one_m_li) {
;     ...
;             float mx = fmaxf(fmaxf(p0[0], p0[1]), p1[0]), mb = fmaxf(fmaxf(p0[2], p0[3]), p1[1]); mx = fmaxf(fmaxf(mx, p1[2]), p1[3]);
; #pragma unroll
;             for (int r = 4; r < 16; r += 4) { mx = fmaxf(fmaxf(mx, p0[r]), p0[r + 1]); mb = fmaxf(fmaxf(mb, p0[r + 2]), p0[r + 3]); mx = fmaxf(fmaxf(mx, p1[r]), p1[r + 1]); mb = fmaxf(fmaxf(mb, p1[r + 2]), p1[r + 3]); }
;             mx = swap_max(fmaxf(mx, mb));
;             if (j == 0 || __any(mx > 8.0f)) {
;                 const float dl = (j == 0) ? mx : fmaxf(mx, 0.f); mrun += dl;
;                 const float alpha = __builtin_amdgcn_exp2f(-dl); lsum *= alpha;
; #pragma unroll
;                 for (int r = 0; r < 16; ++r) { p0[r] -= dl; p1[r] -= dl; negm[r] = -mrun; }
; #pragma unroll
;                 for (int eb = 0; eb < 4; ++eb)
; #pragma unroll
;                     for (int r = 0; r < 16; ++r) o[eb][r] *= alpha;
;             }
.LBB0_590:
	s_nop 7
	v_max_f32_e32 v168, v97, v97
	v_max_f32_e32 v169, v96, v96
	v_max_f32_e32 v168, v169, v168
	v_max3_f32 v169, v98, v99, v81
	v_max3_f32 v168, v168, v80, v82
	v_max3_f32 v168, v168, v83, v100
	v_max3_f32 v169, v169, v102, v103
	v_max3_f32 v168, v168, v101, v84
	v_max3_f32 v169, v169, v86, v87
	v_max3_f32 v168, v168, v85, v104
	v_max3_f32 v169, v169, v106, v107
	v_max3_f32 v168, v168, v105, v88
	v_max3_f32 v169, v169, v90, v91
	v_max3_f32 v168, v168, v89, v108
	v_max3_f32 v169, v169, v110, v111
	v_max3_f32 v168, v168, v109, v92
	v_max3_f32 v169, v169, v94, v95
	v_max3_f32 v168, v168, v93, v169
	s_mov_b32 s8, 0x41000000
	v_cmp_lt_f32_e32 vcc, s8, v168
	s_cbranch_vccz .LBB0_579
	v_mov_b32_e32 v169, v168
	s_nop 1
	v_permlane32_swap_b32 v168, v169
	v_max_f32_e32 v169, v169, v169
	v_max_f32_e32 v168, v168, v168
	v_max_f32_e32 v168, v168, v169
	v_max_f32_e32 v64, v168, v168
	v_max_f32_e32 v66, 0, v64
	v_exp_f32_e64 v68, -v66
	v_add_f32_e32 v162, v162, v66
	v_xor_b32_e32 v64, 0x80000000, v162
	v_pk_add_f32 v[96:97], v[96:97], v[66:67] op_sel_hi:[1,0] neg_lo:[0,1] neg_hi:[0,1]
	v_pk_add_f32 v[80:81], v[80:81], v[66:67] op_sel_hi:[1,0] neg_lo:[0,1] neg_hi:[0,1]
	v_pk_add_f32 v[98:99], v[98:99], v[66:67] op_sel_hi:[1,0] neg_lo:[0,1] neg_hi:[0,1]
	v_pk_add_f32 v[82:83], v[82:83], v[66:67] op_sel_hi:[1,0] neg_lo:[0,1] neg_hi:[0,1]
	v_pk_add_f32 v[100:101], v[100:101], v[66:67] op_sel_hi:[1,0] neg_lo:[0,1] neg_hi:[0,1]
	v_pk_add_f32 v[84:85], v[84:85], v[66:67] op_sel_hi:[1,0] neg_lo:[0,1] neg_hi:[0,1]
	v_pk_add_f32 v[102:103], v[102:103], v[66:67] op_sel_hi:[1,0] neg_lo:[0,1] neg_hi:[0,1]
	v_pk_add_f32 v[86:87], v[86:87], v[66:67] op_sel_hi:[1,0] neg_lo:[0,1] neg_hi:[0,1]
	v_pk_add_f32 v[104:105], v[104:105], v[66:67] op_sel_hi:[1,0] neg_lo:[0,1] neg_hi:[0,1]
	v_pk_add_f32 v[88:89], v[88:89], v[66:67] op_sel_hi:[1,0] neg_lo:[0,1] neg_hi:[0,1]
	v_pk_add_f32 v[106:107], v[106:107], v[66:67] op_sel_hi:[1,0] neg_lo:[0,1] neg_hi:[0,1]
	v_pk_add_f32 v[90:91], v[90:91], v[66:67] op_sel_hi:[1,0] neg_lo:[0,1] neg_hi:[0,1]
	v_pk_add_f32 v[108:109], v[108:109], v[66:67] op_sel_hi:[1,0] neg_lo:[0,1] neg_hi:[0,1]
	v_pk_add_f32 v[92:93], v[92:93], v[66:67] op_sel_hi:[1,0] neg_lo:[0,1] neg_hi:[0,1]
	v_pk_add_f32 v[110:111], v[110:111], v[66:67] op_sel_hi:[1,0] neg_lo:[0,1] neg_hi:[0,1]
	v_pk_add_f32 v[94:95], v[94:95], v[66:67] op_sel_hi:[1,0] neg_lo:[0,1] neg_hi:[0,1]
	v_pk_mul_f32 v[62:63], v[62:63], v[68:69] op_sel_hi:[1,0]
	v_pk_mul_f32 v[60:61], v[60:61], v[68:69] op_sel_hi:[1,0]
	v_pk_mul_f32 v[58:59], v[58:59], v[68:69] op_sel_hi:[1,0]
	v_pk_mul_f32 v[56:57], v[56:57], v[68:69] op_sel_hi:[1,0]
	v_pk_mul_f32 v[54:55], v[54:55], v[68:69] op_sel_hi:[1,0]
	v_pk_mul_f32 v[52:53], v[52:53], v[68:69] op_sel_hi:[1,0]
	v_pk_mul_f32 v[50:51], v[50:51], v[68:69] op_sel_hi:[1,0]
	v_pk_mul_f32 v[48:49], v[48:49], v[68:69] op_sel_hi:[1,0]
	v_pk_mul_f32 v[46:47], v[46:47], v[68:69] op_sel_hi:[1,0]
	v_pk_mul_f32 v[44:45], v[44:45], v[68:69] op_sel_hi:[1,0]
	v_pk_mul_f32 v[42:43], v[42:43], v[68:69] op_sel_hi:[1,0]
	v_pk_mul_f32 v[40:41], v[40:41], v[68:69] op_sel_hi:[1,0]
	v_pk_mul_f32 v[38:39], v[38:39], v[68:69] op_sel_hi:[1,0]
	v_pk_mul_f32 v[36:37], v[36:37], v[68:69] op_sel_hi:[1,0]
	v_pk_mul_f32 v[34:35], v[34:35], v[68:69] op_sel_hi:[1,0]
	v_pk_mul_f32 v[32:33], v[32:33], v[68:69] op_sel_hi:[1,0]
	v_pk_mul_f32 v[30:31], v[30:31], v[68:69] op_sel_hi:[1,0]
	v_pk_mul_f32 v[28:29], v[28:29], v[68:69] op_sel_hi:[1,0]
	v_pk_mul_f32 v[26:27], v[26:27], v[68:69] op_sel_hi:[1,0]
	v_pk_mul_f32 v[24:25], v[24:25], v[68:69] op_sel_hi:[1,0]
	v_pk_mul_f32 v[22:23], v[22:23], v[68:69] op_sel_hi:[1,0]
	v_pk_mul_f32 v[20:21], v[20:21], v[68:69] op_sel_hi:[1,0]
	v_pk_mul_f32 v[18:19], v[18:19], v[68:69] op_sel_hi:[1,0]
	v_pk_mul_f32 v[16:17], v[16:17], v[68:69] op_sel_hi:[1,0]
	v_pk_mul_f32 v[14:15], v[14:15], v[68:69] op_sel_hi:[1,0]
	v_pk_mul_f32 v[12:13], v[12:13], v[68:69] op_sel_hi:[1,0]
	v_pk_mul_f32 v[10:11], v[10:11], v[68:69] op_sel_hi:[1,0]
	v_pk_mul_f32 v[8:9], v[8:9], v[68:69] op_sel_hi:[1,0]
	v_pk_mul_f32 v[6:7], v[6:7], v[68:69] op_sel_hi:[1,0]
	v_pk_mul_f32 v[4:5], v[4:5], v[68:69] op_sel_hi:[1,0]
	v_pk_mul_f32 v[2:3], v[2:3], v[68:69] op_sel_hi:[1,0]
	v_pk_mul_f32 v[0:1], v[0:1], v[68:69] op_sel_hi:[1,0]
	v_mul_f32_e32 v163, v163, v68
	v_mov_b32_e32 v65, v64
	v_mov_b32_e32 v66, v64
	v_mov_b32_e32 v67, v64
	v_mov_b32_e32 v68, v64
	v_mov_b32_e32 v69, v64
	v_mov_b32_e32 v70, v64
	v_mov_b32_e32 v71, v64
	v_mov_b32_e32 v72, v64
	v_mov_b32_e32 v73, v64
	v_mov_b32_e32 v74, v64
	v_mov_b32_e32 v75, v64
	v_mov_b32_e32 v76, v64
	v_mov_b32_e32 v77, v64
	v_mov_b32_e32 v78, v64
	v_mov_b32_e32 v79, v64
	s_branch .LBB0_579
